# stack7_nt_cvnt + non-temporal hint on the MoE gate/up epilogue (HM) stores
# baseline (speedup 1.0000x reference)
; __device__ __forceinline__ float sigmoidf_(float x) { return __builtin_amdgcn_rcpf(1.0f + __expf(-x)); }
;     __device__ __forceinline__ void operator()(g8::Acc& acc, const g8::Unit& u, int wr, int wc, int fr, int fq) const {
;         const int row0 = u.pm * 256 + wr * 64 + fr, col0 = u.pn * 128 + wc * 32 + 8 * fq;
;         const float inv = 1.0f / WGU_SCALE;
; #pragma unroll
;         for (int ai = 0; ai < 2; ++ai)
; #pragma unroll
;             for (int m = 0; m < 4; ++m) { float o[8];
; #pragma unroll
;                 for (int n = 0; n < 2; ++n)
; #pragma unroll
;                     for (int j = 0; j < 4; ++j) { const float gv = acc[ai][0][m][n][j] * inv, uv = acc[ai][1][m][n][j] * inv; o[n * 4 + j] = gv * sigmoidf_(gv) * uv; }
;                 int q0 = 0, q1 = 0;
;                 q0 = __builtin_amdgcn_cvt_pk_fp8_f32(o[0], o[1], q0, false); q0 = __builtin_amdgcn_cvt_pk_fp8_f32(o[2], o[3], q0, true);
;                 q1 = __builtin_amdgcn_cvt_pk_fp8_f32(o[4], o[5], q1, false); q1 = __builtin_amdgcn_cvt_pk_fp8_f32(o[6], o[7], q1, true);
;                 *(u32x2*)(HM + (size_t)(row0 + ai * 128 + m * 16) * 1024 + col0) = (u32x2){(unsigned)q0, (unsigned)q1}; }
;     }
.LBB0_1174:
	s_mov_b32 s4, 0
	v_mov_b32_e32 v3, v130
	v_mbcnt_lo_u32_b32 v2, -1, s4
	v_mbcnt_hi_u32_b32 v5, -1, v2
	v_mov_b32_e32 v2, v98
	v_pk_mul_f32 v[2:3], v[2:3], s[30:31] op_sel_hi:[1,0]
	s_lshl_b32 s4, s82, 8
	v_mul_f32_e32 v6, 0xbfb8aa3b, v2
	v_exp_f32_e32 v7, v6
	s_add_i32 s4, s4, s62
	v_and_or_b32 v4, v5, 15, s4
	s_lshl_b32 s4, s83, 7
	v_lshrrev_b32_e32 v5, 1, v5
	s_or_b32 s4, s4, s63
	v_and_b32_e32 v5, 0x7ffffff8, v5
	v_mov_b32_e32 v8, v99
	v_mov_b32_e32 v9, v131
	v_add_u32_e32 v6, s4, v5
	v_add_f32_e32 v5, 1.0, v7
	v_pk_mul_f32 v[8:9], v[8:9], s[30:31] op_sel_hi:[1,0]
	v_rcp_f32_e32 v5, v5
	v_mul_f32_e32 v7, 0xbfb8aa3b, v8
	v_exp_f32_e32 v10, v7
	v_mov_b32_e32 v11, v133
	v_mul_f32_e32 v2, v2, v5
	v_mul_f32_e32 v5, v2, v3
	v_add_f32_e32 v2, 1.0, v10
	v_rcp_f32_e32 v12, v2
	v_mov_b32_e32 v2, v100
	v_mov_b32_e32 v3, v132
	v_pk_mul_f32 v[2:3], v[2:3], s[30:31] op_sel_hi:[1,0]
	v_mul_f32_e32 v8, v8, v12
	v_mul_f32_e32 v10, 0xbfb8aa3b, v2
	v_exp_f32_e32 v13, v10
	v_mov_b32_e32 v10, v101
	v_pk_mul_f32 v[10:11], v[10:11], s[30:31] op_sel_hi:[1,0]
	v_ashrrev_i32_e32 v7, 31, v6
	v_mul_f32_e32 v14, 0xbfb8aa3b, v10
	v_exp_f32_e32 v14, v14
	v_add_f32_e32 v12, 1.0, v13
	v_rcp_f32_e32 v12, v12
	s_mov_b64 s[4:5], -1
	v_add_f32_e32 v13, 1.0, v14
	v_rcp_f32_e32 v13, v13
	v_mul_f32_e32 v2, v2, v12
	v_mul_f32_e32 v12, v2, v3
	v_mov_b32_e32 v2, v94
	v_mov_b32_e32 v3, v126
	v_pk_mul_f32 v[2:3], v[2:3], s[30:31] op_sel_hi:[1,0]
	v_mul_f32_e32 v14, v8, v9
	v_mul_f32_e32 v8, 0xbfb8aa3b, v2
	v_mul_f32_e32 v10, v10, v13
	v_exp_f32_e32 v13, v8
	v_mov_b32_e32 v8, v95
	v_mov_b32_e32 v9, v127
	v_pk_mul_f32 v[8:9], v[8:9], s[30:31] op_sel_hi:[1,0]
	v_mul_f32_e32 v16, v10, v11
	v_mul_f32_e32 v15, 0xbfb8aa3b, v8
	v_exp_f32_e32 v15, v15
	v_add_f32_e32 v10, 1.0, v13
	v_rcp_f32_e32 v13, v10
	v_mov_b32_e32 v11, v128
	v_add_f32_e32 v10, 1.0, v15
	v_rcp_f32_e32 v15, v10
	v_mov_b32_e32 v10, v96
	v_pk_mul_f32 v[10:11], v[10:11], s[30:31] op_sel_hi:[1,0]
	v_mul_f32_e32 v2, v2, v13
	v_mul_f32_e32 v17, 0xbfb8aa3b, v10
	v_exp_f32_e32 v17, v17
	v_mul_f32_e32 v13, v2, v3
	v_mul_f32_e32 v8, v8, v15
	v_mov_b32_e32 v3, v129
	v_add_f32_e32 v2, 1.0, v17
	v_rcp_f32_e32 v15, v2
	v_mov_b32_e32 v2, v97
	v_pk_mul_f32 v[2:3], v[2:3], s[30:31] op_sel_hi:[1,0]
	v_mul_f32_e32 v18, v8, v9
	v_mul_f32_e32 v17, 0xbfb8aa3b, v2
	v_exp_f32_e32 v17, v17
	v_mul_f32_e32 v8, v10, v15
	v_mul_f32_e32 v10, v8, v11
	v_mov_b32_e32 v9, v67
	v_add_f32_e32 v8, 1.0, v17
	v_rcp_f32_e32 v11, v8
	v_cvt_pk_fp8_f32 v9, v13, v18
	v_mov_b32_e32 v8, v67
	v_cvt_pk_fp8_f32 v8, v5, v14
	v_mul_f32_e32 v2, v2, v11
	v_mul_f32_e32 v2, v2, v3
	v_cvt_pk_fp8_f32 v9, v10, v2 op_sel:[0,0,1]
	v_mov_b32_e32 v2, v90
	v_mov_b32_e32 v3, v122
	v_pk_mul_f32 v[10:11], v[2:3], s[30:31] op_sel_hi:[1,0]
	v_cvt_pk_fp8_f32 v8, v12, v16 op_sel:[0,0,1]
	v_mul_f32_e32 v2, 0xbfb8aa3b, v10
	v_exp_f32_e32 v12, v2
	v_ashrrev_i32_e32 v5, 31, v4
	v_lshlrev_b64 v[2:3], 10, v[4:5]
	v_mov_b32_e32 v13, v123
	v_add_f32_e32 v5, 1.0, v12
	v_mov_b32_e32 v12, v91
	v_pk_mul_f32 v[12:13], v[12:13], s[30:31] op_sel_hi:[1,0]
	v_lshl_add_u64 v[2:3], s[14:15], 0, v[2:3]
	v_mul_f32_e32 v14, 0xbfb8aa3b, v12
	v_exp_f32_e32 v14, v14
	v_lshl_add_u64 v[2:3], v[2:3], 0, v[6:7]
	v_rcp_f32_e32 v5, v5
	global_store_dwordx2 v[2:3], v[8:9], off nt
	v_add_f32_e32 v8, 1.0, v14
	v_rcp_f32_e32 v14, v8
	v_mov_b32_e32 v8, v92
	v_mov_b32_e32 v9, v124
	v_pk_mul_f32 v[8:9], v[8:9], s[30:31] op_sel_hi:[1,0]
	v_mul_f32_e32 v5, v10, v5
	v_mul_f32_e32 v10, 0xbfb8aa3b, v8
	v_exp_f32_e32 v15, v10
	v_mul_f32_e32 v5, v5, v11
	v_mov_b32_e32 v10, v93
	v_mov_b32_e32 v11, v125
	v_pk_mul_f32 v[10:11], v[10:11], s[30:31] op_sel_hi:[1,0]
	v_mul_f32_e32 v12, v12, v14
	v_mul_f32_e32 v16, 0xbfb8aa3b, v10
	v_exp_f32_e32 v16, v16
	v_add_f32_e32 v14, 1.0, v15
	v_rcp_f32_e32 v14, v14
	v_add_f32_e32 v15, 1.0, v16
	v_rcp_f32_e32 v15, v15
	v_mul_f32_e32 v8, v8, v14
	v_mul_f32_e32 v14, v8, v9
	v_mov_b32_e32 v8, v86
	v_mov_b32_e32 v9, v118
	v_pk_mul_f32 v[8:9], v[8:9], s[30:31] op_sel_hi:[1,0]
	v_mul_f32_e32 v16, v12, v13
	v_mul_f32_e32 v12, 0xbfb8aa3b, v8
	v_mul_f32_e32 v10, v10, v15
	v_exp_f32_e32 v15, v12
	v_mov_b32_e32 v12, v87
	v_mov_b32_e32 v13, v119
	v_pk_mul_f32 v[12:13], v[12:13], s[30:31] op_sel_hi:[1,0]
	v_mul_f32_e32 v18, v10, v11
	v_mul_f32_e32 v17, 0xbfb8aa3b, v12
	v_exp_f32_e32 v17, v17
	v_add_f32_e32 v10, 1.0, v15
	v_rcp_f32_e32 v15, v10
	v_mov_b32_e32 v11, v120
	v_add_f32_e32 v10, 1.0, v17
	v_rcp_f32_e32 v17, v10
	v_mov_b32_e32 v10, v88
	v_pk_mul_f32 v[10:11], v[10:11], s[30:31] op_sel_hi:[1,0]
	v_mul_f32_e32 v8, v8, v15
	v_mul_f32_e32 v19, 0xbfb8aa3b, v10
	v_exp_f32_e32 v19, v19
	v_mul_f32_e32 v15, v8, v9
	v_mul_f32_e32 v12, v12, v17
	v_mov_b32_e32 v9, v121
	v_add_f32_e32 v8, 1.0, v19
	v_rcp_f32_e32 v17, v8
	v_mov_b32_e32 v8, v89
	v_pk_mul_f32 v[8:9], v[8:9], s[30:31] op_sel_hi:[1,0]
	v_mul_f32_e32 v12, v12, v13
	v_mul_f32_e32 v19, 0xbfb8aa3b, v8
	v_exp_f32_e32 v19, v19
	v_mul_f32_e32 v10, v10, v17
	v_mul_f32_e32 v13, v10, v11
	v_mov_b32_e32 v11, v67
	v_add_f32_e32 v10, 1.0, v19
	v_rcp_f32_e32 v17, v10
	v_cvt_pk_fp8_f32 v11, v15, v12
	v_mov_b32_e32 v10, v67
	v_cvt_pk_fp8_f32 v10, v5, v16
	v_mul_f32_e32 v5, v8, v17
	v_mul_f32_e32 v5, v5, v9
	v_cvt_pk_fp8_f32 v11, v13, v5 op_sel:[0,0,1]
	v_mov_b32_e32 v12, v82
	v_mov_b32_e32 v13, v114
	v_pk_mul_f32 v[12:13], v[12:13], s[30:31] op_sel_hi:[1,0]
	v_cvt_pk_fp8_f32 v10, v14, v18 op_sel:[0,0,1]
	v_mul_f32_e32 v5, 0xbfb8aa3b, v12
	v_exp_f32_e32 v5, v5
	v_mov_b32_e32 v14, v83
	v_mov_b32_e32 v15, v115
	v_pk_mul_f32 v[14:15], v[14:15], s[30:31] op_sel_hi:[1,0]
	v_or_b32_e32 v8, 16, v4
	v_mul_f32_e32 v16, 0xbfb8aa3b, v14
	v_ashrrev_i32_e32 v9, 31, v8
; __device__ __forceinline__ float sigmoidf_(float x) { return __builtin_amdgcn_rcpf(1.0f + __expf(-x)); }
;     __device__ __forceinline__ void operator()(g8::Acc& acc, const g8::Unit& u, int wr, int wc, int fr, int fq) const {
;         const int row0 = u.pm * 256 + wr * 64 + fr, col0 = u.pn * 128 + wc * 32 + 8 * fq;
;         const float inv = 1.0f / WGU_SCALE;
; #pragma unroll
;         for (int ai = 0; ai < 2; ++ai)
; #pragma unroll
;             for (int m = 0; m < 4; ++m) { float o[8];
; #pragma unroll
;                 for (int n = 0; n < 2; ++n)
; #pragma unroll
;                     for (int j = 0; j < 4; ++j) { const float gv = acc[ai][0][m][n][j] * inv, uv = acc[ai][1][m][n][j] * inv; o[n * 4 + j] = gv * sigmoidf_(gv) * uv; }
;                 int q0 = 0, q1 = 0;
;                 q0 = __builtin_amdgcn_cvt_pk_fp8_f32(o[0], o[1], q0, false); q0 = __builtin_amdgcn_cvt_pk_fp8_f32(o[2], o[3], q0, true);
;                 q1 = __builtin_amdgcn_cvt_pk_fp8_f32(o[4], o[5], q1, false); q1 = __builtin_amdgcn_cvt_pk_fp8_f32(o[6], o[7], q1, true);
;                 *(u32x2*)(HM + (size_t)(row0 + ai * 128 + m * 16) * 1024 + col0) = (u32x2){(unsigned)q0, (unsigned)q1}; }
;     }
	v_add_f32_e32 v5, 1.0, v5
	v_exp_f32_e32 v16, v16
	v_lshlrev_b64 v[8:9], 10, v[8:9]
	v_rcp_f32_e32 v5, v5
	v_lshl_add_u64 v[8:9], s[14:15], 0, v[8:9]
	v_lshl_add_u64 v[8:9], v[8:9], 0, v[6:7]
	global_store_dwordx2 v[8:9], v[10:11], off nt
	v_add_f32_e32 v8, 1.0, v16
	v_mul_f32_e32 v5, v12, v5
	v_rcp_f32_e32 v12, v8
	v_mov_b32_e32 v8, v84
	v_mov_b32_e32 v9, v116
	v_pk_mul_f32 v[8:9], v[8:9], s[30:31] op_sel_hi:[1,0]
	v_mul_f32_e32 v5, v5, v13
	v_mul_f32_e32 v10, 0xbfb8aa3b, v8
	v_exp_f32_e32 v13, v10
	v_mov_b32_e32 v10, v85
	v_mov_b32_e32 v11, v117
	v_pk_mul_f32 v[10:11], v[10:11], s[30:31] op_sel_hi:[1,0]
	v_add_f32_e32 v13, 1.0, v13
	v_mul_f32_e32 v16, 0xbfb8aa3b, v10
	v_exp_f32_e32 v16, v16
	v_rcp_f32_e32 v13, v13
	v_mul_f32_e32 v12, v14, v12
	v_mul_f32_e32 v15, v12, v15
	v_add_f32_e32 v14, 1.0, v16
	v_rcp_f32_e32 v14, v14
	v_mul_f32_e32 v8, v8, v13
	v_mul_f32_e32 v16, v8, v9
	v_mov_b32_e32 v8, v78
	v_mov_b32_e32 v9, v110
	v_pk_mul_f32 v[8:9], v[8:9], s[30:31] op_sel_hi:[1,0]
	v_mul_f32_e32 v10, v10, v14
	v_mul_f32_e32 v12, 0xbfb8aa3b, v8
	v_exp_f32_e32 v14, v12
	v_mov_b32_e32 v12, v79
	v_mov_b32_e32 v13, v111
	v_pk_mul_f32 v[12:13], v[12:13], s[30:31] op_sel_hi:[1,0]
	v_mul_f32_e32 v18, v10, v11
	v_mul_f32_e32 v17, 0xbfb8aa3b, v12
	v_exp_f32_e32 v17, v17
	v_add_f32_e32 v10, 1.0, v14
	v_rcp_f32_e32 v14, v10
	v_mov_b32_e32 v11, v112
	v_add_f32_e32 v10, 1.0, v17
	v_rcp_f32_e32 v17, v10
	v_mov_b32_e32 v10, v80
	v_pk_mul_f32 v[10:11], v[10:11], s[30:31] op_sel_hi:[1,0]
	v_mul_f32_e32 v8, v8, v14
	v_mul_f32_e32 v19, 0xbfb8aa3b, v10
	v_exp_f32_e32 v19, v19
	v_mul_f32_e32 v14, v8, v9
	v_mul_f32_e32 v12, v12, v17
	v_mov_b32_e32 v9, v113
	v_add_f32_e32 v8, 1.0, v19
	v_rcp_f32_e32 v17, v8
	v_mov_b32_e32 v8, v81
	v_pk_mul_f32 v[8:9], v[8:9], s[30:31] op_sel_hi:[1,0]
	v_mul_f32_e32 v12, v12, v13
	v_mul_f32_e32 v19, 0xbfb8aa3b, v8
	v_exp_f32_e32 v19, v19
	v_mul_f32_e32 v10, v10, v17
	v_mul_f32_e32 v13, v10, v11
	v_mov_b32_e32 v11, v67
	v_add_f32_e32 v10, 1.0, v19
	v_rcp_f32_e32 v17, v10
	v_cvt_pk_fp8_f32 v11, v14, v12
	v_mov_b32_e32 v10, v67
	v_cvt_pk_fp8_f32 v10, v5, v15
	v_mul_f32_e32 v5, v8, v17
	v_mul_f32_e32 v5, v5, v9
	v_cvt_pk_fp8_f32 v11, v13, v5 op_sel:[0,0,1]
	v_mov_b32_e32 v12, v74
	v_mov_b32_e32 v13, v106
	v_pk_mul_f32 v[12:13], v[12:13], s[30:31] op_sel_hi:[1,0]
	v_mov_b32_e32 v14, v75
	v_mul_f32_e32 v5, 0xbfb8aa3b, v12
	v_exp_f32_e32 v5, v5
	v_mov_b32_e32 v15, v107
	v_pk_mul_f32 v[14:15], v[14:15], s[30:31] op_sel_hi:[1,0]
	v_cvt_pk_fp8_f32 v10, v16, v18 op_sel:[0,0,1]
	v_or_b32_e32 v8, 32, v4
	v_mul_f32_e32 v16, 0xbfb8aa3b, v14
	v_ashrrev_i32_e32 v9, 31, v8
	v_add_f32_e32 v5, 1.0, v5
	v_exp_f32_e32 v16, v16
	v_lshlrev_b64 v[8:9], 10, v[8:9]
	v_rcp_f32_e32 v5, v5
	v_lshl_add_u64 v[8:9], s[14:15], 0, v[8:9]
	v_lshl_add_u64 v[8:9], v[8:9], 0, v[6:7]
	global_store_dwordx2 v[8:9], v[10:11], off nt
	v_add_f32_e32 v8, 1.0, v16
	v_mul_f32_e32 v5, v12, v5
	v_rcp_f32_e32 v12, v8
	v_mov_b32_e32 v8, v76
	v_mov_b32_e32 v9, v108
	v_pk_mul_f32 v[8:9], v[8:9], s[30:31] op_sel_hi:[1,0]
	v_mul_f32_e32 v5, v5, v13
	v_mul_f32_e32 v10, 0xbfb8aa3b, v8
	v_exp_f32_e32 v13, v10
	v_mov_b32_e32 v10, v77
	v_mov_b32_e32 v11, v109
	v_pk_mul_f32 v[10:11], v[10:11], s[30:31] op_sel_hi:[1,0]
	v_add_f32_e32 v13, 1.0, v13
	v_mul_f32_e32 v16, 0xbfb8aa3b, v10
	v_exp_f32_e32 v16, v16
	v_rcp_f32_e32 v13, v13
	v_mul_f32_e32 v12, v14, v12
	v_mul_f32_e32 v15, v12, v15
	v_add_f32_e32 v14, 1.0, v16
	v_rcp_f32_e32 v14, v14
	v_mul_f32_e32 v8, v8, v13
	v_mul_f32_e32 v16, v8, v9
	v_mov_b32_e32 v8, v70
	v_mov_b32_e32 v9, v102
	v_pk_mul_f32 v[8:9], v[8:9], s[30:31] op_sel_hi:[1,0]
	v_mul_f32_e32 v10, v10, v14
	v_mul_f32_e32 v12, 0xbfb8aa3b, v8
	v_exp_f32_e32 v14, v12
	v_mov_b32_e32 v12, v71
	v_mov_b32_e32 v13, v103
	v_pk_mul_f32 v[12:13], v[12:13], s[30:31] op_sel_hi:[1,0]
	v_mul_f32_e32 v18, v10, v11
	v_mul_f32_e32 v17, 0xbfb8aa3b, v12
	v_exp_f32_e32 v17, v17
	v_add_f32_e32 v10, 1.0, v14
	v_rcp_f32_e32 v14, v10
	v_mov_b32_e32 v11, v104
	v_add_f32_e32 v10, 1.0, v17
	v_rcp_f32_e32 v17, v10
	v_mov_b32_e32 v10, v72
	v_pk_mul_f32 v[10:11], v[10:11], s[30:31] op_sel_hi:[1,0]
	v_mul_f32_e32 v8, v8, v14
	v_mul_f32_e32 v19, 0xbfb8aa3b, v10
	v_exp_f32_e32 v19, v19
	v_mul_f32_e32 v14, v8, v9
	v_mul_f32_e32 v12, v12, v17
	v_mov_b32_e32 v9, v105
	v_add_f32_e32 v8, 1.0, v19
	v_rcp_f32_e32 v17, v8
	v_mov_b32_e32 v8, v73
	v_pk_mul_f32 v[8:9], v[8:9], s[30:31] op_sel_hi:[1,0]
	v_mul_f32_e32 v12, v12, v13
	v_mul_f32_e32 v19, 0xbfb8aa3b, v8
	v_exp_f32_e32 v19, v19
	v_mul_f32_e32 v10, v10, v17
	v_mul_f32_e32 v13, v10, v11
	v_mov_b32_e32 v11, v67
	v_add_f32_e32 v10, 1.0, v19
	v_rcp_f32_e32 v17, v10
	v_mov_b32_e32 v10, v67
	v_cvt_pk_fp8_f32 v10, v5, v15
	v_cvt_pk_fp8_f32 v11, v14, v12
	v_mul_f32_e32 v5, v8, v17
	v_mul_f32_e32 v5, v5, v9
	v_mov_b32_e32 v8, v162
	v_mov_b32_e32 v9, v194
	v_pk_mul_f32 v[8:9], v[8:9], s[30:31] op_sel_hi:[1,0]
	v_or_b32_e32 v4, 48, v4
	v_mul_f32_e32 v12, 0xbfb8aa3b, v8
	v_exp_f32_e32 v12, v12
	v_cvt_pk_fp8_f32 v11, v13, v5 op_sel:[0,0,1]
	v_ashrrev_i32_e32 v5, 31, v4
	v_lshlrev_b64 v[4:5], 10, v[4:5]
	v_lshl_add_u64 v[4:5], s[14:15], 0, v[4:5]
	v_lshl_add_u64 v[4:5], v[4:5], 0, v[6:7]
	v_add_f32_e32 v6, 1.0, v12
	v_rcp_f32_e32 v12, v6
	v_mov_b32_e32 v6, v163
	v_mov_b32_e32 v7, v195
	v_pk_mul_f32 v[6:7], v[6:7], s[30:31] op_sel_hi:[1,0]
	v_cvt_pk_fp8_f32 v10, v16, v18 op_sel:[0,0,1]
	v_mul_f32_e32 v13, 0xbfb8aa3b, v6
	v_exp_f32_e32 v13, v13
	global_store_dwordx2 v[4:5], v[10:11], off nt
	v_mul_f32_e32 v4, v8, v12
	v_mul_f32_e32 v10, v4, v9
	v_add_f32_e32 v4, 1.0, v13
	v_rcp_f32_e32 v11, v4
	v_mov_b32_e32 v4, v164
	v_mov_b32_e32 v5, v196
	v_pk_mul_f32 v[4:5], v[4:5], s[30:31] op_sel_hi:[1,0]
; __device__ __forceinline__ float sigmoidf_(float x) { return __builtin_amdgcn_rcpf(1.0f + __expf(-x)); }
;     __device__ __forceinline__ void operator()(g8::Acc& acc, const g8::Unit& u, int wr, int wc, int fr, int fq) const {
;         const int row0 = u.pm * 256 + wr * 64 + fr, col0 = u.pn * 128 + wc * 32 + 8 * fq;
;         const float inv = 1.0f / WGU_SCALE;
; #pragma unroll
;         for (int ai = 0; ai < 2; ++ai)
; #pragma unroll
;             for (int m = 0; m < 4; ++m) { float o[8];
; #pragma unroll
;                 for (int n = 0; n < 2; ++n)
; #pragma unroll
;                     for (int j = 0; j < 4; ++j) { const float gv = acc[ai][0][m][n][j] * inv, uv = acc[ai][1][m][n][j] * inv; o[n * 4 + j] = gv * sigmoidf_(gv) * uv; }
;                 int q0 = 0, q1 = 0;
;                 q0 = __builtin_amdgcn_cvt_pk_fp8_f32(o[0], o[1], q0, false); q0 = __builtin_amdgcn_cvt_pk_fp8_f32(o[2], o[3], q0, true);
;                 q1 = __builtin_amdgcn_cvt_pk_fp8_f32(o[4], o[5], q1, false); q1 = __builtin_amdgcn_cvt_pk_fp8_f32(o[6], o[7], q1, true);
;                 *(u32x2*)(HM + (size_t)(row0 + ai * 128 + m * 16) * 1024 + col0) = (u32x2){(unsigned)q0, (unsigned)q1}; }
;     }
	v_mov_b32_e32 v9, v197
	v_mul_f32_e32 v8, 0xbfb8aa3b, v4
	v_exp_f32_e32 v12, v8
	v_mov_b32_e32 v8, v165
	v_pk_mul_f32 v[8:9], v[8:9], s[30:31] op_sel_hi:[1,0]
	v_mul_f32_e32 v6, v6, v11
	v_mul_f32_e32 v13, 0xbfb8aa3b, v8
	v_exp_f32_e32 v13, v13
	v_add_f32_e32 v11, 1.0, v12
	v_rcp_f32_e32 v11, v11
	v_add_f32_e32 v12, 1.0, v13
	v_rcp_f32_e32 v12, v12
	v_mul_f32_e32 v4, v4, v11
	v_mul_f32_e32 v11, v4, v5
	v_mov_b32_e32 v4, v158
	v_mov_b32_e32 v5, v190
	v_pk_mul_f32 v[4:5], v[4:5], s[30:31] op_sel_hi:[1,0]
	v_mul_f32_e32 v13, v6, v7
	v_mul_f32_e32 v6, 0xbfb8aa3b, v4
	v_mul_f32_e32 v8, v8, v12
	v_exp_f32_e32 v12, v6
	v_mov_b32_e32 v6, v159
	v_mov_b32_e32 v7, v191
	v_pk_mul_f32 v[6:7], v[6:7], s[30:31] op_sel_hi:[1,0]
	v_mul_f32_e32 v15, v8, v9
	v_mul_f32_e32 v14, 0xbfb8aa3b, v6
	v_exp_f32_e32 v14, v14
	v_add_f32_e32 v8, 1.0, v12
	v_rcp_f32_e32 v12, v8
	v_mov_b32_e32 v9, v192
	v_add_f32_e32 v8, 1.0, v14
	v_rcp_f32_e32 v14, v8
	v_mov_b32_e32 v8, v160
	v_pk_mul_f32 v[8:9], v[8:9], s[30:31] op_sel_hi:[1,0]
	v_mul_f32_e32 v4, v4, v12
	v_mul_f32_e32 v16, 0xbfb8aa3b, v8
	v_exp_f32_e32 v16, v16
	v_mul_f32_e32 v12, v4, v5
	v_mul_f32_e32 v6, v6, v14
	v_mov_b32_e32 v5, v193
	v_add_f32_e32 v4, 1.0, v16
	v_rcp_f32_e32 v14, v4
	v_mov_b32_e32 v4, v161
	v_pk_mul_f32 v[4:5], v[4:5], s[30:31] op_sel_hi:[1,0]
	v_mul_f32_e32 v17, v6, v7
	v_mul_f32_e32 v16, 0xbfb8aa3b, v4
	v_exp_f32_e32 v16, v16
	v_mul_f32_e32 v6, v8, v14
	v_mul_f32_e32 v8, v6, v9
	v_mov_b32_e32 v7, v67
	v_add_f32_e32 v6, 1.0, v16
	v_rcp_f32_e32 v9, v6
	v_cvt_pk_fp8_f32 v7, v12, v17
	v_mov_b32_e32 v6, v67
	v_cvt_pk_fp8_f32 v6, v10, v13
	v_mul_f32_e32 v4, v4, v9
	v_mul_f32_e32 v4, v4, v5
	v_cvt_pk_fp8_f32 v7, v8, v4 op_sel:[0,0,1]
	v_mov_b32_e32 v4, v154
	v_mov_b32_e32 v5, v186
	v_pk_mul_f32 v[4:5], v[4:5], s[30:31] op_sel_hi:[1,0]
	v_cvt_pk_fp8_f32 v6, v11, v15 op_sel:[0,0,1]
	v_mul_f32_e32 v8, 0xbfb8aa3b, v4
	v_exp_f32_e32 v10, v8
	v_mov_b32_e32 v11, v187
	v_add_co_u32_e32 v8, vcc, s71, v2
	v_add_f32_e32 v10, 1.0, v10
	v_rcp_f32_e32 v12, v10
	v_mov_b32_e32 v10, v155
	v_pk_mul_f32 v[10:11], v[10:11], s[30:31] op_sel_hi:[1,0]
	v_addc_co_u32_e32 v9, vcc, 0, v3, vcc
	v_mul_f32_e32 v13, 0xbfb8aa3b, v10
	v_exp_f32_e32 v13, v13
	v_mul_f32_e32 v4, v4, v12
	v_mul_f32_e32 v12, v4, v5
	global_store_dwordx2 v[8:9], v[6:7], off nt
	v_add_f32_e32 v4, 1.0, v13
	v_rcp_f32_e32 v8, v4
	v_mov_b32_e32 v4, v156
	v_mov_b32_e32 v5, v188
	v_pk_mul_f32 v[4:5], v[4:5], s[30:31] op_sel_hi:[1,0]
	v_mov_b32_e32 v7, v189
	v_mul_f32_e32 v6, 0xbfb8aa3b, v4
	v_exp_f32_e32 v9, v6
	v_mov_b32_e32 v6, v157
	v_pk_mul_f32 v[6:7], v[6:7], s[30:31] op_sel_hi:[1,0]
	v_mul_f32_e32 v8, v10, v8
	v_mul_f32_e32 v13, 0xbfb8aa3b, v6
	v_exp_f32_e32 v13, v13
	v_add_f32_e32 v9, 1.0, v9
	v_rcp_f32_e32 v9, v9
	v_mul_f32_e32 v11, v8, v11
	v_add_f32_e32 v10, 1.0, v13
	v_rcp_f32_e32 v10, v10
	v_mul_f32_e32 v4, v4, v9
	v_mul_f32_e32 v13, v4, v5
	v_mov_b32_e32 v4, v150
	v_mov_b32_e32 v5, v182
	v_pk_mul_f32 v[4:5], v[4:5], s[30:31] op_sel_hi:[1,0]
	v_mul_f32_e32 v6, v6, v10
	v_mul_f32_e32 v8, 0xbfb8aa3b, v4
	v_exp_f32_e32 v10, v8
	v_mov_b32_e32 v8, v151
	v_mov_b32_e32 v9, v183
	v_pk_mul_f32 v[8:9], v[8:9], s[30:31] op_sel_hi:[1,0]
	v_mul_f32_e32 v15, v6, v7
	v_mul_f32_e32 v14, 0xbfb8aa3b, v8
	v_exp_f32_e32 v14, v14
	v_add_f32_e32 v6, 1.0, v10
	v_rcp_f32_e32 v10, v6
	v_mov_b32_e32 v7, v184
	v_add_f32_e32 v6, 1.0, v14
	v_rcp_f32_e32 v14, v6
	v_mov_b32_e32 v6, v152
	v_pk_mul_f32 v[6:7], v[6:7], s[30:31] op_sel_hi:[1,0]
	v_mul_f32_e32 v4, v4, v10
	v_mul_f32_e32 v16, 0xbfb8aa3b, v6
	v_exp_f32_e32 v16, v16
	v_mul_f32_e32 v10, v4, v5
	v_mul_f32_e32 v8, v8, v14
	v_mov_b32_e32 v5, v185
	v_add_f32_e32 v4, 1.0, v16
	v_rcp_f32_e32 v14, v4
	v_mov_b32_e32 v4, v153
	v_pk_mul_f32 v[4:5], v[4:5], s[30:31] op_sel_hi:[1,0]
	v_mul_f32_e32 v8, v8, v9
	v_mul_f32_e32 v16, 0xbfb8aa3b, v4
	v_exp_f32_e32 v16, v16
	v_mul_f32_e32 v6, v6, v14
	v_mul_f32_e32 v9, v6, v7
	v_mov_b32_e32 v7, v67
	v_add_f32_e32 v6, 1.0, v16
	v_rcp_f32_e32 v14, v6
	v_cvt_pk_fp8_f32 v7, v10, v8
	v_mov_b32_e32 v6, v67
	v_cvt_pk_fp8_f32 v6, v12, v11
	v_mul_f32_e32 v4, v4, v14
	v_mul_f32_e32 v4, v4, v5
	v_cvt_pk_fp8_f32 v7, v9, v4 op_sel:[0,0,1]
	v_mov_b32_e32 v4, v146
	v_mov_b32_e32 v5, v178
	v_pk_mul_f32 v[4:5], v[4:5], s[30:31] op_sel_hi:[1,0]
	v_mov_b32_e32 v11, v179
	v_mul_f32_e32 v8, 0xbfb8aa3b, v4
	v_exp_f32_e32 v10, v8
	v_cvt_pk_fp8_f32 v6, v13, v15 op_sel:[0,0,1]
	v_add_co_u32_e32 v8, vcc, s72, v2
	v_add_f32_e32 v10, 1.0, v10
	v_rcp_f32_e32 v12, v10
	v_mov_b32_e32 v10, v147
	v_pk_mul_f32 v[10:11], v[10:11], s[30:31] op_sel_hi:[1,0]
	v_addc_co_u32_e32 v9, vcc, 0, v3, vcc
	v_mul_f32_e32 v13, 0xbfb8aa3b, v10
	v_exp_f32_e32 v13, v13
	v_mul_f32_e32 v4, v4, v12
	v_mul_f32_e32 v12, v4, v5
	global_store_dwordx2 v[8:9], v[6:7], off nt
	v_add_f32_e32 v4, 1.0, v13
	v_rcp_f32_e32 v8, v4
	v_mov_b32_e32 v4, v148
	v_mov_b32_e32 v5, v180
	v_pk_mul_f32 v[4:5], v[4:5], s[30:31] op_sel_hi:[1,0]
	v_mov_b32_e32 v7, v181
	v_mul_f32_e32 v6, 0xbfb8aa3b, v4
	v_exp_f32_e32 v9, v6
	v_mov_b32_e32 v6, v149
	v_pk_mul_f32 v[6:7], v[6:7], s[30:31] op_sel_hi:[1,0]
	v_mul_f32_e32 v8, v10, v8
	v_mul_f32_e32 v13, 0xbfb8aa3b, v6
	v_exp_f32_e32 v13, v13
	v_add_f32_e32 v9, 1.0, v9
	v_rcp_f32_e32 v9, v9
	v_mul_f32_e32 v11, v8, v11
	v_add_f32_e32 v10, 1.0, v13
	v_rcp_f32_e32 v10, v10
	v_mul_f32_e32 v4, v4, v9
	v_mul_f32_e32 v13, v4, v5
	v_mov_b32_e32 v4, v142
	v_mov_b32_e32 v5, v174
	v_pk_mul_f32 v[4:5], v[4:5], s[30:31] op_sel_hi:[1,0]
	v_mul_f32_e32 v6, v6, v10
	v_mul_f32_e32 v8, 0xbfb8aa3b, v4
	v_exp_f32_e32 v10, v8
	v_mov_b32_e32 v8, v143
	v_mov_b32_e32 v9, v175
	v_pk_mul_f32 v[8:9], v[8:9], s[30:31] op_sel_hi:[1,0]
	v_mul_f32_e32 v15, v6, v7
; __device__ __forceinline__ float sigmoidf_(float x) { return __builtin_amdgcn_rcpf(1.0f + __expf(-x)); }
;     ...
;         if (!has_next) break;
;         if (!(cur.flags & 1)) {
; #pragma unroll
;             for (int a = 0; a < 2; ++a)
; #pragma unroll
;                 for (int b = 0; b < 2; ++b)
; #pragma unroll
;                     for (int m = 0; m < 4; ++m)
; #pragma unroll
;                         for (int n = 0; n < 2; ++n) acc[a][b][m][n] = (f32x4){0.f, 0.f, 0.f, 0.f};
;         }
;     __device__ __forceinline__ void operator()(g8::Acc& acc, const g8::Unit& u, int wr, int wc, int fr, int fq) const {
;         const int row0 = u.pm * 256 + wr * 64 + fr, col0 = u.pn * 128 + wc * 32 + 8 * fq;
;         const float inv = 1.0f / WGU_SCALE;
; #pragma unroll
;         for (int ai = 0; ai < 2; ++ai)
; #pragma unroll
;             for (int m = 0; m < 4; ++m) { float o[8];
; #pragma unroll
;                 for (int n = 0; n < 2; ++n)
; #pragma unroll
;                     for (int j = 0; j < 4; ++j) { const float gv = acc[ai][0][m][n][j] * inv, uv = acc[ai][1][m][n][j] * inv; o[n * 4 + j] = gv * sigmoidf_(gv) * uv; }
;                 int q0 = 0, q1 = 0;
;                 q0 = __builtin_amdgcn_cvt_pk_fp8_f32(o[0], o[1], q0, false); q0 = __builtin_amdgcn_cvt_pk_fp8_f32(o[2], o[3], q0, true);
;                 q1 = __builtin_amdgcn_cvt_pk_fp8_f32(o[4], o[5], q1, false); q1 = __builtin_amdgcn_cvt_pk_fp8_f32(o[6], o[7], q1, true);
;                 *(u32x2*)(HM + (size_t)(row0 + ai * 128 + m * 16) * 1024 + col0) = (u32x2){(unsigned)q0, (unsigned)q1}; }
;     }
	v_mul_f32_e32 v14, 0xbfb8aa3b, v8
	v_exp_f32_e32 v14, v14
	v_add_f32_e32 v6, 1.0, v10
	v_rcp_f32_e32 v10, v6
	v_mov_b32_e32 v7, v176
	v_add_f32_e32 v6, 1.0, v14
	v_rcp_f32_e32 v14, v6
	v_mov_b32_e32 v6, v144
	v_pk_mul_f32 v[6:7], v[6:7], s[30:31] op_sel_hi:[1,0]
	v_mul_f32_e32 v4, v4, v10
	v_mul_f32_e32 v16, 0xbfb8aa3b, v6
	v_exp_f32_e32 v16, v16
	v_mul_f32_e32 v10, v4, v5
	v_mul_f32_e32 v8, v8, v14
	v_mov_b32_e32 v5, v177
	v_add_f32_e32 v4, 1.0, v16
	v_rcp_f32_e32 v14, v4
	v_mov_b32_e32 v4, v145
	v_pk_mul_f32 v[4:5], v[4:5], s[30:31] op_sel_hi:[1,0]
	v_mul_f32_e32 v8, v8, v9
	v_mul_f32_e32 v16, 0xbfb8aa3b, v4
	v_exp_f32_e32 v16, v16
	v_mul_f32_e32 v6, v6, v14
	v_mul_f32_e32 v9, v6, v7
	v_mov_b32_e32 v7, v67
	v_add_f32_e32 v6, 1.0, v16
	v_rcp_f32_e32 v14, v6
	v_cvt_pk_fp8_f32 v7, v10, v8
	v_mov_b32_e32 v6, v67
	v_cvt_pk_fp8_f32 v6, v12, v11
	v_mul_f32_e32 v4, v4, v14
	v_mul_f32_e32 v4, v4, v5
	v_cvt_pk_fp8_f32 v7, v9, v4 op_sel:[0,0,1]
	v_mov_b32_e32 v4, v138
	v_mov_b32_e32 v5, v170
	v_pk_mul_f32 v[4:5], v[4:5], s[30:31] op_sel_hi:[1,0]
	v_mov_b32_e32 v11, v171
	v_mul_f32_e32 v8, 0xbfb8aa3b, v4
	v_exp_f32_e32 v10, v8
	v_cvt_pk_fp8_f32 v6, v13, v15 op_sel:[0,0,1]
	v_add_co_u32_e32 v8, vcc, s73, v2
	v_add_f32_e32 v10, 1.0, v10
	v_rcp_f32_e32 v12, v10
	v_mov_b32_e32 v10, v139
	v_pk_mul_f32 v[10:11], v[10:11], s[30:31] op_sel_hi:[1,0]
	v_addc_co_u32_e32 v9, vcc, 0, v3, vcc
	v_mul_f32_e32 v13, 0xbfb8aa3b, v10
	v_exp_f32_e32 v13, v13
	v_mul_f32_e32 v4, v4, v12
	v_mul_f32_e32 v12, v4, v5
	global_store_dwordx2 v[8:9], v[6:7], off nt
	v_add_f32_e32 v4, 1.0, v13
	v_rcp_f32_e32 v8, v4
	v_mov_b32_e32 v4, v140
	v_mov_b32_e32 v5, v172
	v_pk_mul_f32 v[4:5], v[4:5], s[30:31] op_sel_hi:[1,0]
	v_mov_b32_e32 v7, v173
	v_mul_f32_e32 v6, 0xbfb8aa3b, v4
	v_exp_f32_e32 v9, v6
	v_mov_b32_e32 v6, v141
	v_pk_mul_f32 v[6:7], v[6:7], s[30:31] op_sel_hi:[1,0]
	v_mul_f32_e32 v8, v10, v8
	v_mul_f32_e32 v13, 0xbfb8aa3b, v6
	v_exp_f32_e32 v13, v13
	v_add_f32_e32 v9, 1.0, v9
	v_rcp_f32_e32 v9, v9
	v_mul_f32_e32 v11, v8, v11
	v_add_f32_e32 v10, 1.0, v13
	v_rcp_f32_e32 v10, v10
	v_mul_f32_e32 v4, v4, v9
	v_mul_f32_e32 v13, v4, v5
	v_mov_b32_e32 v4, v134
	v_mov_b32_e32 v5, v166
	v_pk_mul_f32 v[4:5], v[4:5], s[30:31] op_sel_hi:[1,0]
	v_mul_f32_e32 v6, v6, v10
	v_mul_f32_e32 v8, 0xbfb8aa3b, v4
	v_exp_f32_e32 v10, v8
	v_mov_b32_e32 v8, v135
	v_mov_b32_e32 v9, v167
	v_pk_mul_f32 v[8:9], v[8:9], s[30:31] op_sel_hi:[1,0]
	v_mul_f32_e32 v15, v6, v7
	v_mul_f32_e32 v14, 0xbfb8aa3b, v8
	v_exp_f32_e32 v14, v14
	v_add_f32_e32 v6, 1.0, v10
	v_rcp_f32_e32 v10, v6
	v_mov_b32_e32 v7, v168
	v_add_f32_e32 v6, 1.0, v14
	v_rcp_f32_e32 v14, v6
	v_mov_b32_e32 v6, v136
	v_pk_mul_f32 v[6:7], v[6:7], s[30:31] op_sel_hi:[1,0]
	v_mul_f32_e32 v4, v4, v10
	v_mul_f32_e32 v16, 0xbfb8aa3b, v6
	v_exp_f32_e32 v16, v16
	v_mul_f32_e32 v10, v4, v5
	v_mul_f32_e32 v8, v8, v14
	v_mov_b32_e32 v5, v169
	v_add_f32_e32 v4, 1.0, v16
	v_rcp_f32_e32 v14, v4
	v_mov_b32_e32 v4, v137
	v_pk_mul_f32 v[4:5], v[4:5], s[30:31] op_sel_hi:[1,0]
	v_mul_f32_e32 v8, v8, v9
	v_mul_f32_e32 v16, 0xbfb8aa3b, v4
	v_exp_f32_e32 v16, v16
	v_mul_f32_e32 v6, v6, v14
	v_mul_f32_e32 v9, v6, v7
	v_mov_b32_e32 v7, v67
	v_add_f32_e32 v6, 1.0, v16
	v_rcp_f32_e32 v14, v6
	v_mov_b32_e32 v6, v67
	v_cvt_pk_fp8_f32 v6, v12, v11
	v_cvt_pk_fp8_f32 v7, v10, v8
	v_mul_f32_e32 v4, v4, v14
	v_mul_f32_e32 v4, v4, v5
	v_cvt_pk_fp8_f32 v6, v13, v15 op_sel:[0,0,1]
	v_cvt_pk_fp8_f32 v7, v9, v4 op_sel:[0,0,1]
	v_add_co_u32_e32 v2, vcc, 0x2c000, v2
	s_nop 1
	v_addc_co_u32_e32 v3, vcc, 0, v3, vcc
	s_and_b64 vcc, exec, s[36:37]
	global_store_dwordx2 v[2:3], v[6:7], off nt
	s_cbranch_vccz .LBB0_1135
	s_bitcmp1_b32 s81, 0
	s_cselect_b64 s[4:5], -1, 0
	s_and_b64 vcc, exec, s[4:5]
	s_cbranch_vccnz .LBB0_1134
	v_mov_b32_e32 v68, v67
	v_mov_b32_e32 v69, v67
	v_mov_b32_e32 v66, v67
	v_mov_b64_e32 v[100:101], v[68:69]
	v_mov_b64_e32 v[96:97], v[68:69]
	v_mov_b64_e32 v[92:93], v[68:69]
	v_mov_b64_e32 v[88:89], v[68:69]
	v_mov_b64_e32 v[84:85], v[68:69]
	v_mov_b64_e32 v[80:81], v[68:69]
	v_mov_b64_e32 v[76:77], v[68:69]
	v_mov_b64_e32 v[72:73], v[68:69]
	v_mov_b64_e32 v[132:133], v[68:69]
	v_mov_b64_e32 v[128:129], v[68:69]
	v_mov_b64_e32 v[124:125], v[68:69]
	v_mov_b64_e32 v[120:121], v[68:69]
	v_mov_b64_e32 v[116:117], v[68:69]
	v_mov_b64_e32 v[112:113], v[68:69]
	v_mov_b64_e32 v[108:109], v[68:69]
	v_mov_b64_e32 v[104:105], v[68:69]
	v_mov_b64_e32 v[164:165], v[68:69]
	v_mov_b64_e32 v[160:161], v[68:69]
	v_mov_b64_e32 v[156:157], v[68:69]
	v_mov_b64_e32 v[152:153], v[68:69]
	v_mov_b64_e32 v[148:149], v[68:69]
	v_mov_b64_e32 v[144:145], v[68:69]
	v_mov_b64_e32 v[140:141], v[68:69]
	v_mov_b64_e32 v[136:137], v[68:69]
	v_mov_b64_e32 v[196:197], v[68:69]
	v_mov_b64_e32 v[192:193], v[68:69]
	v_mov_b64_e32 v[188:189], v[68:69]
	v_mov_b64_e32 v[184:185], v[68:69]
	v_mov_b64_e32 v[180:181], v[68:69]
	v_mov_b64_e32 v[176:177], v[68:69]
	v_mov_b64_e32 v[172:173], v[68:69]
	v_mov_b64_e32 v[168:169], v[68:69]
	v_mov_b64_e32 v[98:99], v[66:67]
	v_mov_b64_e32 v[94:95], v[66:67]
	v_mov_b64_e32 v[90:91], v[66:67]
	v_mov_b64_e32 v[86:87], v[66:67]
	v_mov_b64_e32 v[82:83], v[66:67]
	v_mov_b64_e32 v[78:79], v[66:67]
	v_mov_b64_e32 v[74:75], v[66:67]
	v_mov_b64_e32 v[70:71], v[66:67]
	v_mov_b64_e32 v[130:131], v[66:67]
	v_mov_b64_e32 v[126:127], v[66:67]
	v_mov_b64_e32 v[122:123], v[66:67]
	v_mov_b64_e32 v[118:119], v[66:67]
	v_mov_b64_e32 v[114:115], v[66:67]
	v_mov_b64_e32 v[110:111], v[66:67]
	v_mov_b64_e32 v[106:107], v[66:67]
	v_mov_b64_e32 v[102:103], v[66:67]
	v_mov_b64_e32 v[162:163], v[66:67]
	v_mov_b64_e32 v[158:159], v[66:67]
	v_mov_b64_e32 v[154:155], v[66:67]
	v_mov_b64_e32 v[150:151], v[66:67]
	v_mov_b64_e32 v[146:147], v[66:67]
	v_mov_b64_e32 v[142:143], v[66:67]
	v_mov_b64_e32 v[138:139], v[66:67]
	v_mov_b64_e32 v[134:135], v[66:67]
	v_mov_b64_e32 v[194:195], v[66:67]
	v_mov_b64_e32 v[190:191], v[66:67]
	v_mov_b64_e32 v[186:187], v[66:67]
	v_mov_b64_e32 v[182:183], v[66:67]
	v_mov_b64_e32 v[178:179], v[66:67]
	v_mov_b64_e32 v[174:175], v[66:67]
	v_mov_b64_e32 v[170:171], v[66:67]
	v_mov_b64_e32 v[166:167], v[66:67]
	s_branch .LBB0_1134
